# mLSTM gate GEMV loop software-pipelined (16 loads issued ahead, counted vmcnt) on top of gather depth7+3 barriers
# speedup vs baseline: 1.0120x; 1.0055x over previous
; __device__ __forceinline__ void ph_mlstm_gates(const Frame& F, int j) {
;     ...
;     for (int task = F.gw; task < T / 16; task += F.ngw) {
;         const bf16* xa = XB + (size_t)(task * 16 + l15) * D + 8 * g;
;         const bf16* wb = WGB + (size_t)l15 * 2048 + 8 * g;
;         f32x4 a0 = (f32x4){0.f, 0.f, 0.f, 0.f}, a1 = a0;
; #pragma unroll 4
;         for (int st = 0; st < 64; st += 2) {
;             a0 = __builtin_amdgcn_mfma_f32_16x16x32_bf16(*(const bf16x8*)(xa + 32 * st), *(const bf16x8*)(wb + 32 * st), a0, 0, 0, 0);
;             a1 = __builtin_amdgcn_mfma_f32_16x16x32_bf16(*(const bf16x8*)(xa + 32 * st + 32), *(const bf16x8*)(wb + 32 * st + 32), a1, 0, 0, 0);
;         }
; #pragma unroll
;         for (int i = 0; i < 4; ++i) GA[(size_t)(task * 16 + 4 * g + i) * 16 + l15] = a0[i] + a1[i];
;     }
.LBB0_314:
	v_lshl_add_u64 v[24:25], v[18:19], 0, v[12:13]
	v_add_co_u32_e32 v32, vcc, 0x36600000, v24
	v_lshl_add_u64 v[34:35], v[20:21], 0, v[12:13]
	s_nop 0
	v_addc_co_u32_e32 v33, vcc, 0, v25, vcc
	global_load_dwordx4 v[40:43], v[32:33], off
	global_load_dwordx4 v[72:75], v[34:35], off offset:-256
	global_load_dwordx4 v[44:47], v[32:33], off offset:64
	global_load_dwordx4 v[76:79], v[34:35], off offset:-192
	global_load_dwordx4 v[48:51], v[32:33], off offset:128
	global_load_dwordx4 v[80:83], v[34:35], off offset:-128
	global_load_dwordx4 v[52:55], v[32:33], off offset:192
	global_load_dwordx4 v[84:87], v[34:35], off offset:-64
	global_load_dwordx4 v[56:59], v[32:33], off offset:256
	global_load_dwordx4 v[88:91], v[34:35], off
	global_load_dwordx4 v[60:63], v[32:33], off offset:320
	global_load_dwordx4 v[92:95], v[34:35], off offset:64
	global_load_dwordx4 v[64:67], v[32:33], off offset:384
	global_load_dwordx4 v[96:99], v[34:35], off offset:128
	global_load_dwordx4 v[68:71], v[32:33], off offset:448
	global_load_dwordx4 v[100:103], v[34:35], off offset:192
	s_mov_b32 s4, 0
.Lgt_loop:
	global_load_dwordx4 v[104:107], v[32:33], off offset:512
	global_load_dwordx4 v[212:215], v[34:35], off offset:256
	global_load_dwordx4 v[108:111], v[32:33], off offset:576
	global_load_dwordx4 v[216:219], v[34:35], off offset:320
	global_load_dwordx4 v[112:115], v[32:33], off offset:640
	global_load_dwordx4 v[220:223], v[34:35], off offset:384
	global_load_dwordx4 v[116:119], v[32:33], off offset:704
	global_load_dwordx4 v[224:227], v[34:35], off offset:448
	global_load_dwordx4 v[120:123], v[32:33], off offset:768
	global_load_dwordx4 v[228:231], v[34:35], off offset:512
	global_load_dwordx4 v[124:127], v[32:33], off offset:832
	global_load_dwordx4 v[232:235], v[34:35], off offset:576
	global_load_dwordx4 v[128:131], v[32:33], off offset:896
	global_load_dwordx4 v[236:239], v[34:35], off offset:640
	global_load_dwordx4 v[132:135], v[32:33], off offset:960
	global_load_dwordx4 v[240:243], v[34:35], off offset:704
	s_waitcnt vmcnt(30)
	v_mfma_f32_16x16x32_bf16 v[2:5], v[40:43], v[72:75], v[2:5]
	s_waitcnt vmcnt(28)
	v_mfma_f32_16x16x32_bf16 v[6:9], v[44:47], v[76:79], v[6:9]
	s_waitcnt vmcnt(26)
	v_mfma_f32_16x16x32_bf16 v[2:5], v[48:51], v[80:83], v[2:5]
	s_waitcnt vmcnt(24)
	v_mfma_f32_16x16x32_bf16 v[6:9], v[52:55], v[84:87], v[6:9]
	s_waitcnt vmcnt(22)
	v_mfma_f32_16x16x32_bf16 v[2:5], v[56:59], v[88:91], v[2:5]
	s_waitcnt vmcnt(20)
	v_mfma_f32_16x16x32_bf16 v[6:9], v[60:63], v[92:95], v[6:9]
	s_waitcnt vmcnt(18)
	v_mfma_f32_16x16x32_bf16 v[2:5], v[64:67], v[96:99], v[2:5]
	s_waitcnt vmcnt(16)
	v_mfma_f32_16x16x32_bf16 v[6:9], v[68:71], v[100:103], v[6:9]
	global_load_dwordx4 v[40:43], v[32:33], off offset:1024
	global_load_dwordx4 v[72:75], v[34:35], off offset:768
	global_load_dwordx4 v[44:47], v[32:33], off offset:1088
	global_load_dwordx4 v[76:79], v[34:35], off offset:832
	global_load_dwordx4 v[48:51], v[32:33], off offset:1152
	global_load_dwordx4 v[80:83], v[34:35], off offset:896
	global_load_dwordx4 v[52:55], v[32:33], off offset:1216
	global_load_dwordx4 v[84:87], v[34:35], off offset:960
	global_load_dwordx4 v[56:59], v[32:33], off offset:1280
	global_load_dwordx4 v[88:91], v[34:35], off offset:1024
	global_load_dwordx4 v[60:63], v[32:33], off offset:1344
	global_load_dwordx4 v[92:95], v[34:35], off offset:1088
	global_load_dwordx4 v[64:67], v[32:33], off offset:1408
	global_load_dwordx4 v[96:99], v[34:35], off offset:1152
	global_load_dwordx4 v[68:71], v[32:33], off offset:1472
	global_load_dwordx4 v[100:103], v[34:35], off offset:1216
	s_waitcnt vmcnt(30)
	v_mfma_f32_16x16x32_bf16 v[2:5], v[104:107], v[212:215], v[2:5]
	s_waitcnt vmcnt(28)
	v_mfma_f32_16x16x32_bf16 v[6:9], v[108:111], v[216:219], v[6:9]
	s_waitcnt vmcnt(26)
	v_mfma_f32_16x16x32_bf16 v[2:5], v[112:115], v[220:223], v[2:5]
	s_waitcnt vmcnt(24)
	v_mfma_f32_16x16x32_bf16 v[6:9], v[116:119], v[224:227], v[6:9]
	s_waitcnt vmcnt(22)
	v_mfma_f32_16x16x32_bf16 v[2:5], v[120:123], v[228:231], v[2:5]
	s_waitcnt vmcnt(20)
	v_mfma_f32_16x16x32_bf16 v[6:9], v[124:127], v[232:235], v[6:9]
	s_waitcnt vmcnt(18)
	v_mfma_f32_16x16x32_bf16 v[2:5], v[128:131], v[236:239], v[2:5]
	s_waitcnt vmcnt(16)
	v_mfma_f32_16x16x32_bf16 v[6:9], v[132:135], v[240:243], v[6:9]
	v_lshl_add_u64 v[32:33], s[96:97], 1, v[32:33]
	v_lshl_add_u64 v[34:35], s[96:97], 1, v[34:35]
	s_add_i32 s4, s4, 1
	s_cmp_lt_u32 s4, 4
	s_cbranch_scc1 .Lgt_loop
	s_waitcnt vmcnt(0)
	v_lshl_add_u32 v18, s1, 4, v22
	v_ashrrev_i32_e32 v19, 31, v18
	v_lshlrev_b64 v[20:21], 6, v[18:19]
	s_nop 3
	v_add_f32_e32 v0, v2, v6
	v_lshl_add_u64 v[20:21], v[10:11], 0, v[20:21]
	v_or_b32_e32 v2, 1, v18
	global_store_dword v[20:21], v0, off
	v_add_f32_e32 v0, v3, v7
	v_ashrrev_i32_e32 v3, 31, v2
	v_lshlrev_b64 v[2:3], 6, v[2:3]
	v_lshl_add_u64 v[2:3], v[10:11], 0, v[2:3]
	global_store_dword v[2:3], v0, off
	v_or_b32_e32 v2, 2, v18
	v_ashrrev_i32_e32 v3, 31, v2
	v_lshlrev_b64 v[2:3], 6, v[2:3]
	v_add_f32_e32 v0, v4, v8
	v_lshl_add_u64 v[2:3], v[10:11], 0, v[2:3]
	global_store_dword v[2:3], v0, off
	v_or_b32_e32 v2, 3, v18
	v_ashrrev_i32_e32 v3, 31, v2
	v_lshlrev_b64 v[2:3], 6, v[2:3]
	s_add_i32 s1, s1, s76
	v_add_f32_e32 v0, v5, v9
	v_lshl_add_u64 v[2:3], v[10:11], 0, v[2:3]
	s_cmpk_gt_i32 s1, 0x3ff
	v_add_u32_e32 v16, s0, v16
	global_store_dword v[2:3], v0, off
	s_cbranch_scc0 .LBB0_313
